# baseline (speedup 1.0000x reference)
.LBB1_57:
	v_add_u32_e32 v0, s2, v191
	v_add3_u32 v197, v0, v209, v210
	v_max_f32_e32 v0, v33, v33
	v_max_f32_e32 v2, v32, v32
	v_max_f32_e32 v0, v2, v0
	v_max3_f32 v2, v34, v35, v17
	v_max3_f32 v0, v0, v16, v18
	v_max3_f32 v0, v0, v19, v36
	v_max3_f32 v2, v2, v38, v39
	v_max3_f32 v0, v0, v37, v20
	v_max3_f32 v2, v2, v22, v23
	v_max3_f32 v0, v0, v21, v40
	v_max3_f32 v2, v2, v42, v43
	v_max3_f32 v0, v0, v41, v24
	v_max3_f32 v2, v2, v26, v27
	v_max3_f32 v0, v0, v25, v44
	v_max3_f32 v2, v2, v46, v47
	v_max3_f32 v0, v0, v45, v28
	v_max3_f32 v2, v2, v30, v31
	v_max3_f32 v0, v0, v29, v2
	v_mov_b32_e32 v2, v0
	s_and_b32 s3, s23, 0x3fffffc0
	s_nop 0
	v_permlane32_swap_b32_e32 v0, v2
	s_lshl_b32 s2, s3, 2
	v_max_f32_e32 v2, v2, v2
	v_max_f32_e32 v0, v0, v0
	s_add_i32 s27, s2, 0
	v_max_f32_e32 v0, v0, v2
	s_mov_b32 s2, 0x41000000
	v_cmp_le_f32_e32 vcc, -4.0, v0
	v_cmp_ge_f32_e64 s[2:3], s2, v0
	v_max_f32_e32 v0, 0xf149f2ca, v0
	s_and_b64 s[2:3], vcc, s[2:3]
	v_cndmask_b32_e64 v192, v0, 0, s[2:3]
	v_add_f32_e64 v0, v32, -v192
	v_exp_f32_e32 v64, v0
	v_add_f32_e64 v0, v16, -v192
	v_exp_f32_e32 v32, v0
	v_add_f32_e64 v0, v33, -v192
	v_exp_f32_e32 v65, v0
	v_add_f32_e64 v0, v17, -v192
	v_exp_f32_e32 v33, v0
	v_add_f32_e64 v0, v34, -v192
	v_exp_f32_e32 v66, v0
	v_add_f32_e64 v0, v18, -v192
	v_exp_f32_e32 v34, v0
	v_add_f32_e64 v0, v35, -v192
	v_exp_f32_e32 v67, v0
	v_add_f32_e64 v0, v19, -v192
	v_exp_f32_e32 v35, v0
	v_add_f32_e64 v0, v36, -v192
	v_exp_f32_e32 v68, v0
	v_add_f32_e64 v0, v20, -v192
	v_exp_f32_e32 v36, v0
	v_add_f32_e64 v0, v37, -v192
	v_exp_f32_e32 v69, v0
	v_add_f32_e64 v0, v21, -v192
	v_exp_f32_e32 v37, v0
	v_add_f32_e64 v0, v38, -v192
	v_exp_f32_e32 v70, v0
	v_add_f32_e64 v0, v22, -v192
	v_exp_f32_e32 v38, v0
	v_add_f32_e64 v0, v39, -v192
	v_exp_f32_e32 v71, v0
	v_add_f32_e64 v0, v23, -v192
	v_exp_f32_e32 v39, v0
	v_add_f32_e64 v0, v40, -v192
	v_exp_f32_e32 v72, v0
	v_add_f32_e64 v0, v24, -v192
	v_exp_f32_e32 v40, v0
	v_add_f32_e64 v0, v41, -v192
	v_exp_f32_e32 v73, v0
	v_add_f32_e64 v0, v25, -v192
	v_exp_f32_e32 v41, v0
	v_add_f32_e64 v0, v42, -v192
	v_exp_f32_e32 v74, v0
	v_add_f32_e64 v0, v26, -v192
	v_exp_f32_e32 v42, v0
	v_add_f32_e64 v0, v43, -v192
	v_exp_f32_e32 v75, v0
	v_add_f32_e64 v0, v27, -v192
	v_exp_f32_e32 v43, v0
	v_add_f32_e64 v0, v44, -v192
	v_exp_f32_e32 v76, v0
	v_add_f32_e64 v0, v28, -v192
	v_exp_f32_e32 v44, v0
	v_add_f32_e64 v0, v45, -v192
	v_exp_f32_e32 v77, v0
	v_add_f32_e64 v0, v29, -v192
	v_exp_f32_e32 v45, v0
	v_add_f32_e64 v0, v46, -v192
	v_exp_f32_e32 v78, v0
	v_add_f32_e64 v0, v30, -v192
	v_exp_f32_e32 v46, v0
	v_add_f32_e64 v0, v47, -v192
	v_exp_f32_e32 v79, v0
	v_add_f32_e64 v0, v31, -v192
	v_exp_f32_e32 v47, v0
	s_bitcmp1_b32 s36, 8
	s_cbranch_scc1 .Lu2w_g1
	s_waitcnt vmcnt(2) lgkmcnt(0)
	s_branch .Lu2w_done
.Lu2w_g1:
	s_waitcnt vmcnt(2) lgkmcnt(0)
